# kernel-entry de-serialisation: the conditioning vector c is requested in front of the first workgroup barrier (pointer fetched with the first kernarg group) instead of after the kernarg/spill prologue
# speedup vs baseline: 1.0033x; 1.0028x over previous
_Z4mega5MArgs:
	s_load_dwordx4 s[28:31], s[0:1], 0xe0
	s_load_dword s33, s[0:1], 0xf0
	s_load_dwordx2 s[100:101], s[0:1], 0x8
	v_lshlrev_b32_e32 v150, 2, v0
	v_add_u32_e32 v151, 0x1000, v150
	s_add_u32 s4, s0, 0xf0
	s_addc_u32 s5, s1, 0
	v_lshrrev_b32_e32 v1, 6, v0
	s_nop 1
	v_readfirstlane_b32 s98, v1
	v_and_b32_e32 v1, 63, v0
	v_writelane_b32 v249, s4, 0
	v_cmp_eq_u32_e32 vcc, 0, v1
	s_nop 0
	v_writelane_b32 v249, s5, 1
	s_and_saveexec_b64 s[4:5], vcc
	s_cbranch_execz .LBB0_2
	s_getreg_b32 s3, hwreg(HW_REG_HW_ID, 0, 6)
	s_lshl_b32 s3, s3, 2
	s_and_b32 s3, s3, 0xfc
	s_add_i32 s3, s3, 0
	s_add_i32 s3, s3, 0x25c00
	v_lshrrev_b32_e32 v1, 6, v0
	v_mov_b32_e32 v2, s3
	ds_write_b32 v2, v1
.LBB0_2:
	s_or_b64 exec, exec, s[4:5]
	s_load_dwordx8 s[72:79], s[0:1], 0xc0
	v_cmp_gt_u32_e32 vcc, 5, v0
	s_and_saveexec_b64 s[4:5], vcc
	v_lshl_add_u32 v0, v0, 2, 0
	v_add_u32_e32 v0, 0x24800, v0
	v_mov_b32_e32 v1, 0
	ds_write_b32 v0, v1
	s_or_b64 exec, exec, s[4:5]
	s_waitcnt lgkmcnt(0)
	global_load_dword v140, v150, s[100:101]
	global_load_dword v141, v150, s[100:101] offset:2048
	global_load_dword v142, v151, s[100:101]
	global_load_dword v143, v151, s[100:101] offset:2048
	s_mul_i32 s4, s30, 0xd80
	s_ashr_i32 s5, s4, 31
	s_lshl_b64 s[4:5], s[4:5], 2
	s_add_u32 s3, s78, s4
	s_addc_u32 s4, s79, s5
	s_add_u32 s94, s3, 0x4000
	s_barrier
	s_addc_u32 s95, s4, 0
	s_getreg_b32 s3, hwreg(HW_REG_XCC_ID, 0, 4)
	s_getreg_b32 s4, hwreg(HW_REG_HW_ID, 0, 6)
	s_lshl_b32 s4, s4, 2
	s_and_b32 s4, s4, 0xfc
	s_add_i32 s4, s4, 0
	s_add_i32 s4, s4, 0x25c00
	v_mov_b32_e32 v0, s4
	s_load_dwordx16 s[4:19], s[0:1], 0x0
	ds_read_b32 v0, v0
	s_and_b32 s3, s3, 15
	s_waitcnt lgkmcnt(0)
	v_writelane_b32 v249, s4, 2
	s_nop 1
	v_writelane_b32 v249, s5, 3
	v_writelane_b32 v249, s6, 4
	v_writelane_b32 v249, s7, 5
	v_writelane_b32 v249, s8, 6
	v_writelane_b32 v249, s9, 7
	v_writelane_b32 v249, s10, 8
	v_writelane_b32 v249, s11, 9
	v_writelane_b32 v249, s12, 10
	v_writelane_b32 v249, s13, 11
	v_writelane_b32 v249, s14, 12
	v_writelane_b32 v249, s15, 13
	v_writelane_b32 v249, s16, 14
	v_writelane_b32 v249, s17, 15
	v_writelane_b32 v249, s18, 16
	v_writelane_b32 v249, s19, 17
	s_load_dwordx16 s[4:19], s[0:1], 0x40
	s_waitcnt lgkmcnt(0)
	v_writelane_b32 v249, s4, 18
	s_nop 1
	v_writelane_b32 v249, s5, 19
	v_writelane_b32 v249, s6, 20
	v_writelane_b32 v249, s7, 21
	v_writelane_b32 v249, s8, 22
	v_writelane_b32 v249, s9, 23
	v_writelane_b32 v249, s10, 24
	v_writelane_b32 v249, s11, 25
	v_writelane_b32 v249, s12, 26
	v_writelane_b32 v249, s13, 27
	v_writelane_b32 v249, s14, 28
	v_writelane_b32 v249, s15, 29
	v_writelane_b32 v249, s16, 30
	v_writelane_b32 v249, s17, 31
	v_writelane_b32 v249, s18, 32
	v_writelane_b32 v249, s19, 33
	v_writelane_b32 v249, s3, 34
	v_readfirstlane_b32 s3, v0
	v_mbcnt_lo_u32_b32 v0, -1, 0
	v_mbcnt_hi_u32_b32 v0, -1, v0
	s_nop 1
	v_lshl_add_u32 v0, s3, 6, v0
	s_nop 0
	v_cmp_eq_u32_e32 vcc, 0, v0
	s_and_saveexec_b64 s[4:5], vcc
	s_cbranch_execz .LBB0_7
	s_mov_b64 s[6:7], exec
	v_mbcnt_lo_u32_b32 v0, s6, 0
	v_mbcnt_hi_u32_b32 v0, s7, v0
	v_cmp_eq_u32_e32 vcc, 0, v0
	s_and_b64 s[8:9], exec, vcc
	s_mov_b64 exec, s[8:9]
	s_cbranch_execz .LBB0_7
	v_readlane_b32 s3, v249, 34
	s_lshl_b32 s3, s3, 8
	s_bcnt1_i32_b64 s6, s[6:7]
	v_mov_b32_e32 v0, s3
	v_mov_b32_e32 v1, s6
	global_atomic_add v0, v1, s[94:95] offset:1024
.LBB0_7:
	s_or_b64 exec, exec, s[4:5]
	s_load_dwordx16 s[4:19], s[0:1], 0x80
	s_add_u32 s96, s78, 0x40000
	s_addc_u32 s97, s79, 0
	s_add_u32 s90, s78, 0x8500000
	s_addc_u32 s91, s79, 0
	s_waitcnt lgkmcnt(0)
	v_writelane_b32 v249, s4, 35
	s_cmp_lt_i32 s28, 1
	s_cselect_b64 s[0:1], -1, 0
	v_writelane_b32 v249, s5, 36
	v_writelane_b32 v249, s6, 37
	v_writelane_b32 v249, s7, 38
	v_writelane_b32 v249, s8, 39
	v_writelane_b32 v249, s9, 40
	v_writelane_b32 v249, s10, 41
	v_writelane_b32 v249, s11, 42
	v_writelane_b32 v249, s12, 43
	v_writelane_b32 v249, s13, 44
	v_writelane_b32 v249, s14, 45
	v_writelane_b32 v249, s15, 46
	v_writelane_b32 v249, s16, 47
	v_writelane_b32 v249, s17, 48
	v_writelane_b32 v249, s18, 49
	s_cmp_gt_i32 s29, 0
	v_writelane_b32 v249, s19, 50
	s_cselect_b64 s[4:5], -1, 0
	s_and_b64 s[0:1], s[0:1], s[4:5]
	s_andn2_b64 vcc, exec, s[0:1]
	s_cbranch_vccnz .LBB0_90
	v_mbcnt_lo_u32_b32 v1, -1, 0
	v_mbcnt_hi_u32_b32 v1, -1, v1
	s_cmpk_gt_i32 s2, 0xbf
	s_waitcnt lgkmcnt(0)
	s_mov_b32 s0, s98
	s_nop 1
	v_lshl_add_u32 v28, s0, 6, v1
	s_nop 0
	v_ashrrev_i32_e32 v23, 6, v28
	v_and_b32_e32 v30, 63, v28
	s_cbranch_scc1 .LBB0_18
	v_readlane_b32 s4, v249, 2
	v_readlane_b32 s6, v249, 4
	v_readlane_b32 s7, v249, 5
	v_ashrrev_i32_e32 v29, 31, v28
	v_mov_b32_e32 v0, s6
	v_mov_b32_e32 v1, s7
	v_lshl_add_u64 v[0:1], v[28:29], 2, v[0:1]
	s_waitcnt vmcnt(0)
	v_mov_b32_e32 v2, v140
	v_mov_b32_e32 v3, v141
	s_movk_i32 s0, 0x1000
	v_add_co_u32_e32 v0, vcc, s0, v0
	s_mov_b32 s0, 0xbfb8aa3b
	s_nop 0
	v_addc_co_u32_e32 v1, vcc, 0, v1, vcc
	v_mov_b32_e32 v4, v142
	s_nop 0
	v_mov_b32_e32 v0, v143
	s_mov_b32 s3, 0x42ce8ed0
	s_mov_b32 s6, 0xc2b17218
	v_mov_b32_e32 v1, 0x7f800000
	v_readlane_b32 s5, v249, 3
	v_lshl_add_u32 v5, v28, 2, 0
	v_readlane_b32 s8, v249, 6
	v_readlane_b32 s9, v249, 7
	v_readlane_b32 s10, v249, 8
	v_readlane_b32 s11, v249, 9
	v_readlane_b32 s14, v249, 12
	v_mov_b32_e32 v33, 0
	v_lshlrev_b32_e32 v32, 2, v30
	s_mov_b32 s14, s2
	v_readlane_b32 s12, v249, 10
	v_readlane_b32 s13, v249, 11
	v_readlane_b32 s15, v249, 13
	v_readlane_b32 s16, v249, 14
	v_readlane_b32 s17, v249, 15
	v_readlane_b32 s18, v249, 16
	v_readlane_b32 s19, v249, 17
	s_waitcnt vmcnt(3)
	v_mul_f32_e32 v6, 0xbfb8aa3b, v2
	s_waitcnt vmcnt(2)
	v_mul_f32_e32 v7, 0xbfb8aa3b, v3
	v_fma_f32 v8, v2, s0, -v6
	v_rndne_f32_e32 v9, v6
	v_fma_f32 v10, v3, s0, -v7
	v_rndne_f32_e32 v11, v7
	v_fmac_f32_e32 v8, 0xb2a5705f, v2
	v_sub_f32_e32 v6, v6, v9
	v_fmac_f32_e32 v10, 0xb2a5705f, v3
	v_sub_f32_e32 v7, v7, v11
	v_add_f32_e32 v6, v6, v8
	s_waitcnt vmcnt(1)
	v_mul_f32_e32 v12, 0xbfb8aa3b, v4
	v_cvt_i32_f32_e32 v9, v9
	v_add_f32_e32 v7, v7, v10
	v_exp_f32_e32 v6, v6
	v_cvt_i32_f32_e32 v11, v11
	v_fma_f32 v14, v4, s0, -v12
	v_rndne_f32_e32 v15, v12
	v_exp_f32_e32 v7, v7
	v_fmac_f32_e32 v14, 0xb2a5705f, v4
	v_sub_f32_e32 v8, v12, v15
	s_waitcnt vmcnt(0)
	v_mul_f32_e32 v13, 0xbfb8aa3b, v0
	v_add_f32_e32 v8, v8, v14
	v_fma_f32 v16, v0, s0, -v13
	v_rndne_f32_e32 v17, v13
	v_cvt_i32_f32_e32 v10, v15
	v_exp_f32_e32 v8, v8
	v_ldexp_f32 v6, v6, v9
	v_cmp_nlt_f32_e32 vcc, s3, v2
	v_fmac_f32_e32 v16, 0xb2a5705f, v0
	v_sub_f32_e32 v12, v13, v17
	v_ldexp_f32 v7, v7, v11
	v_cndmask_b32_e32 v6, 0, v6, vcc
	v_cmp_nlt_f32_e32 vcc, s3, v3
	v_add_f32_e32 v12, v12, v16
	v_cvt_i32_f32_e32 v13, v17
	v_cndmask_b32_e32 v7, 0, v7, vcc
	v_cmp_ngt_f32_e32 vcc, s6, v2
	v_exp_f32_e32 v12, v12
	v_ldexp_f32 v8, v8, v10
	v_cndmask_b32_e32 v6, v1, v6, vcc
	v_cmp_ngt_f32_e32 vcc, s6, v3
	v_add_f32_e32 v6, 1.0, v6
	v_div_scale_f32 v10, s[0:1], v6, v6, v2
	v_cndmask_b32_e32 v7, v1, v7, vcc
	v_cmp_nlt_f32_e32 vcc, s3, v4
	v_add_f32_e32 v7, 1.0, v7
	v_ldexp_f32 v9, v12, v13
	v_cndmask_b32_e32 v8, 0, v8, vcc
	v_cmp_ngt_f32_e32 vcc, s6, v4
	v_div_scale_f32 v12, s[0:1], v7, v7, v3
	s_nop 0
	v_cndmask_b32_e32 v8, v1, v8, vcc
	v_add_f32_e32 v8, 1.0, v8
	v_rcp_f32_e32 v14, v10
	v_rcp_f32_e32 v15, v12
	v_div_scale_f32 v16, s[4:5], v8, v8, v4
	v_rcp_f32_e32 v18, v16
	v_fma_f32 v19, -v10, v14, 1.0
	v_div_scale_f32 v11, vcc, v2, v6, v2
	v_fma_f32 v20, -v12, v15, 1.0
	v_fmac_f32_e32 v14, v19, v14
	v_div_scale_f32 v13, s[0:1], v3, v7, v3
	v_fmac_f32_e32 v15, v20, v15
	v_fma_f32 v19, -v16, v18, 1.0
	v_mul_f32_e32 v20, v11, v14
	v_mul_f32_e32 v21, v13, v15
	v_fmac_f32_e32 v18, v19, v18
	v_fma_f32 v19, -v10, v20, v11
	v_fma_f32 v22, -v12, v21, v13
	v_fmac_f32_e32 v20, v19, v14
	v_fmac_f32_e32 v21, v22, v15
	v_fma_f32 v10, -v10, v20, v11
	v_fma_f32 v11, -v12, v21, v13
	v_div_fmas_f32 v10, v10, v14, v20
	s_mov_b64 vcc, s[0:1]
	v_div_fixup_f32 v2, v10, v6, v2
	v_div_fmas_f32 v6, v11, v15, v21
	v_div_fixup_f32 v3, v6, v7, v3
	v_cmp_nlt_f32_e32 vcc, s3, v0
	ds_write2st64_b32 v5, v2, v3 offset1:8
	v_div_scale_f32 v17, s[4:5], v4, v8, v4
	v_cndmask_b32_e32 v2, 0, v9, vcc
	v_cmp_ngt_f32_e32 vcc, s6, v0
	v_mul_f32_e32 v24, v17, v18
	v_fma_f32 v19, -v16, v24, v17
	v_cndmask_b32_e32 v1, v1, v2, vcc
	v_add_f32_e32 v1, 1.0, v1
	v_div_scale_f32 v2, s[0:1], v1, v1, v0
	v_rcp_f32_e32 v3, v2
	v_fmac_f32_e32 v24, v19, v18
	v_fma_f32 v12, -v16, v24, v17
	s_mov_b64 vcc, s[4:5]
	v_div_fmas_f32 v6, v12, v18, v24
	v_div_fixup_f32 v4, v6, v8, v4
	v_fma_f32 v6, -v2, v3, 1.0
	v_fmac_f32_e32 v3, v6, v3
	v_div_scale_f32 v6, vcc, v0, v1, v0
	v_mul_f32_e32 v7, v6, v3
	v_fma_f32 v8, -v2, v7, v6
	v_fmac_f32_e32 v7, v8, v3
	v_fma_f32 v2, -v2, v7, v6
	v_div_fmas_f32 v2, v2, v3, v7
	v_div_fixup_f32 v0, v2, v1, v0
	v_lshlrev_b32_e32 v2, 2, v30
	ds_write2st64_b32 v5, v4, v0 offset0:16 offset1:24
	v_add_u32_e32 v0, 0, v2
	v_lshlrev_b32_e32 v3, 9, v23
	v_lshlrev_b32_e32 v1, 7, v23
	v_add_u32_e32 v27, 0, v3
	v_add_u32_e32 v29, v0, v3
	v_and_b32_e32 v3, 0x3fffffc0, v28
	s_movk_i32 s3, 0x6000
	v_lshl_add_u32 v31, v3, 2, v0
	v_mad_i64_i32 v[0:1], s[8:9], v1, s3, 0
	v_or_b32_e32 v0, v0, v2
	s_add_u32 s6, s78, 0x8200
	s_movk_i32 s0, 0x80
	v_lshl_add_u64 v[0:1], s[10:11], 0, v[0:1]
	s_mov_b64 s[8:9], 0xba000
	s_addc_u32 s7, s79, 0
	v_cmp_gt_i32_e64 s[0:1], s0, v28
	v_cmp_eq_u32_e64 s[4:5], 0, v28
	v_lshl_add_u64 v[34:35], v[0:1], 0, s[8:9]
	s_mov_b64 s[8:9], 0xc0000
	s_waitcnt lgkmcnt(0)
	s_barrier
	s_branch .LBB0_11
